# speedup vs baseline: 1.0037x; 1.0037x over previous
.Lkb2_done:
	v_max_f32_e32 v129, v156, v157
	s_nop 0
	v_mov_b32_e32 v131, v129
	s_nop 1
	v_permlane32_swap_b32_e32 v129, v131
	v_max_f32_e32 v129, v129, v131
	v_mfma_f32_32x32x16_bf16 a[16:31], v[132:135], v[140:143], a[16:31]
	v_max_f32_e32 v128, v128, v130
	v_mov_b32_e32 v130, v128
	s_nop 1
	v_permlane32_swap_b32_e32 v128, v130
	v_max_f32_e32 v128, v128, v130
	v_max_f32_e32 v130, v129, v128
	v_mfma_f32_32x32x16_bf16 a[32:47], v[60:63], v[52:55], a[32:47]
	v_cmp_lt_f32_e32 vcc, s31, v130
	s_cmp_lg_u64 vcc, 0
	s_cselect_b64 s[0:1], -1, 0
	s_cbranch_vccnz .LBB0_22
.LBB0_18:
	v_cvt_pk_bf16_f32 v156, v227, v228
	v_cvt_pk_bf16_f32 v157, v229, v230
	v_cvt_pk_bf16_f32 v158, v231, v232
	v_cvt_pk_bf16_f32 v159, v233, v234
	v_cvt_pk_bf16_f32 v160, v148, v149
	v_cvt_pk_bf16_f32 v161, v150, v151
	v_cvt_pk_bf16_f32 v162, v152, v153
	v_cvt_pk_bf16_f32 v163, v154, v155
	v_exp_f32_e32 v128, v112
	v_exp_f32_e32 v129, v113
	v_mfma_f32_32x32x16_bf16 a[48:63], v[60:63], v[140:143], a[48:63]
	v_exp_f32_e32 v130, v114
	v_exp_f32_e32 v131, v115
	v_mfma_f32_32x32x16_bf16 a[64:79], v[56:59], v[52:55], a[64:79]
	v_exp_f32_e32 v132, v116
	v_exp_f32_e32 v133, v117
	v_exp_f32_e32 v134, v118
	v_mfma_f32_32x32x16_bf16 a[80:95], v[56:59], v[140:143], a[80:95]
	v_add_f32_e32 v56, v128, v130
	v_add_f32_e32 v57, v129, v131
	v_exp_f32_e32 v135, v119
	v_exp_f32_e32 v136, v120
	v_mfma_f32_32x32x16_bf16 a[96:111], v[48:51], v[52:55], a[96:111]
	v_add_f32_e32 v52, v56, v132
	v_add_f32_e32 v53, v57, v133
	v_add_f32_e32 v52, v52, v134
	v_exp_f32_e32 v137, v121
	v_exp_f32_e32 v138, v122
	v_exp_f32_e32 v139, v123
	v_mfma_f32_32x32x16_bf16 a[112:127], v[48:51], v[140:143], a[112:127]
	v_add_f32_e32 v48, v53, v135
	v_add_f32_e32 v49, v52, v136
	v_exp_f32_e32 v140, v124
	v_exp_f32_e32 v141, v125
	v_mfma_f32_32x32x16_bf16 a[0:15], v[44:47], v[156:159], a[0:15]
	v_add_f32_e32 v48, v48, v137
	v_add_f32_e32 v49, v49, v138
	v_add_f32_e32 v48, v48, v139
	v_exp_f32_e32 v142, v126
	v_exp_f32_e32 v143, v127
	v_exp_f32_e32 v144, v96
	v_mfma_f32_32x32x16_bf16 a[16:31], v[44:47], v[160:163], a[16:31]
	v_add_f32_e32 v44, v49, v140
	v_add_f32_e32 v45, v48, v141
	v_exp_f32_e32 v145, v97
	v_exp_f32_e32 v146, v98
	v_mfma_f32_32x32x16_bf16 a[32:47], v[40:43], v[156:159], a[32:47]
	v_add_f32_e32 v236, v44, v142
	v_add_f32_e32 v235, v45, v143
	v_exp_f32_e32 v147, v99
	v_exp_f32_e32 v148, v100
	v_exp_f32_e32 v149, v101
	v_mfma_f32_32x32x16_bf16 a[48:63], v[40:43], v[160:163], a[48:63]
	v_add_f32_e32 v41, v144, v146
	v_exp_f32_e32 v150, v102
	v_exp_f32_e32 v151, v103
	v_mfma_f32_32x32x16_bf16 a[64:79], v[36:39], v[156:159], a[64:79]
	v_add_f32_e32 v40, v145, v147
	v_add_f32_e32 v41, v41, v148
	v_add_f32_e32 v40, v40, v149
	v_exp_f32_e32 v152, v104
	v_exp_f32_e32 v153, v105
	v_exp_f32_e32 v154, v106
	v_mfma_f32_32x32x16_bf16 a[80:95], v[36:39], v[160:163], a[80:95]
	v_add_f32_e32 v36, v41, v150
	v_add_f32_e32 v37, v40, v151
	v_mfma_f32_32x32x16_bf16 a[96:111], v[32:35], v[156:159], a[96:111]
	v_exp_f32_e32 v155, v107
	v_exp_f32_e32 v156, v108
	v_add_f32_e32 v36, v36, v152
	v_add_f32_e32 v37, v37, v153
	v_add_f32_e32 v36, v36, v154
	v_exp_f32_e32 v157, v109
	v_exp_f32_e32 v158, v110
	v_exp_f32_e32 v159, v111
	v_mfma_f32_32x32x16_bf16 a[112:127], v[32:35], v[160:163], a[112:127]
	v_add_f32_e32 v32, v37, v155
	v_add_f32_e32 v33, v36, v156
	s_andn2_b64 vcc, exec, s[0:1]
	v_add_f32_e32 v32, v32, v157
	v_add_f32_e32 v237, v33, v158
	s_nop 0
	v_add_f32_e32 v238, v32, v159
	s_cbranch_vccz .LBB0_23

.Lkd2_done:
	v_max_f32_e32 v129, v156, v157
	s_nop 0
	v_mov_b32_e32 v131, v129
	s_nop 1
	v_permlane32_swap_b32_e32 v129, v131
	v_max_f32_e32 v129, v129, v131
	v_mfma_f32_32x32x16_bf16 a[16:31], v[132:135], v[140:143], a[16:31]
	v_max_f32_e32 v128, v128, v130
	v_mov_b32_e32 v130, v128
	s_nop 1
	v_permlane32_swap_b32_e32 v128, v130
	v_max_f32_e32 v128, v128, v130
	v_max_f32_e32 v130, v129, v128
	v_mfma_f32_32x32x16_bf16 a[32:47], v[92:95], v[84:87], a[32:47]
	v_cmp_lt_f32_e32 vcc, s31, v130
	s_cmp_lg_u64 vcc, 0
	s_cselect_b64 s[0:1], -1, 0
	s_cbranch_vccnz .LBB0_24
.LBB0_20:
	v_cvt_pk_bf16_f32 v156, v227, v228
	v_cvt_pk_bf16_f32 v157, v229, v230
	v_cvt_pk_bf16_f32 v158, v231, v232
	v_cvt_pk_bf16_f32 v159, v233, v234
	v_cvt_pk_bf16_f32 v160, v148, v149
	v_cvt_pk_bf16_f32 v161, v150, v151
	v_cvt_pk_bf16_f32 v162, v152, v153
	v_cvt_pk_bf16_f32 v163, v154, v155
	v_exp_f32_e32 v128, v112
	v_exp_f32_e32 v129, v113
	v_mfma_f32_32x32x16_bf16 a[48:63], v[92:95], v[140:143], a[48:63]
	v_exp_f32_e32 v130, v114
	v_exp_f32_e32 v131, v115
	v_mfma_f32_32x32x16_bf16 a[64:79], v[88:91], v[84:87], a[64:79]
	v_exp_f32_e32 v132, v116
	v_exp_f32_e32 v133, v117
	v_exp_f32_e32 v134, v118
	v_mfma_f32_32x32x16_bf16 a[80:95], v[88:91], v[140:143], a[80:95]
	v_add_f32_e32 v88, v128, v130
	v_add_f32_e32 v89, v129, v131
	v_exp_f32_e32 v135, v119
	v_exp_f32_e32 v136, v120
	v_mfma_f32_32x32x16_bf16 a[96:111], v[80:83], v[84:87], a[96:111]
	v_add_f32_e32 v84, v88, v132
	v_add_f32_e32 v85, v89, v133
	v_add_f32_e32 v84, v84, v134
	v_exp_f32_e32 v137, v121
	v_exp_f32_e32 v138, v122
	v_exp_f32_e32 v139, v123
	v_mfma_f32_32x32x16_bf16 a[112:127], v[80:83], v[140:143], a[112:127]
	v_add_f32_e32 v80, v85, v135
	v_add_f32_e32 v81, v84, v136
	v_exp_f32_e32 v140, v124
	v_exp_f32_e32 v141, v125
	v_mfma_f32_32x32x16_bf16 a[0:15], v[76:79], v[156:159], a[0:15]
	v_add_f32_e32 v80, v80, v137
	v_add_f32_e32 v81, v81, v138
	v_add_f32_e32 v80, v80, v139
	v_exp_f32_e32 v142, v126
	v_exp_f32_e32 v143, v127
	v_exp_f32_e32 v144, v96
	v_mfma_f32_32x32x16_bf16 a[16:31], v[76:79], v[160:163], a[16:31]
	v_add_f32_e32 v76, v81, v140
	v_add_f32_e32 v77, v80, v141
	v_exp_f32_e32 v145, v97
	v_exp_f32_e32 v146, v98
	v_mfma_f32_32x32x16_bf16 a[32:47], v[72:75], v[156:159], a[32:47]
	v_add_f32_e32 v236, v76, v142
	v_add_f32_e32 v235, v77, v143
	v_exp_f32_e32 v147, v99
	v_exp_f32_e32 v148, v100
	v_exp_f32_e32 v149, v101
	v_mfma_f32_32x32x16_bf16 a[48:63], v[72:75], v[160:163], a[48:63]
	v_add_f32_e32 v73, v144, v146
	v_exp_f32_e32 v150, v102
	v_exp_f32_e32 v151, v103
	v_mfma_f32_32x32x16_bf16 a[64:79], v[68:71], v[156:159], a[64:79]
	v_add_f32_e32 v72, v145, v147
	v_add_f32_e32 v73, v73, v148
	v_add_f32_e32 v72, v72, v149
	v_exp_f32_e32 v152, v104
	v_exp_f32_e32 v153, v105
	v_exp_f32_e32 v154, v106
	v_mfma_f32_32x32x16_bf16 a[80:95], v[68:71], v[160:163], a[80:95]
	v_add_f32_e32 v68, v73, v150
	v_add_f32_e32 v69, v72, v151
	v_mfma_f32_32x32x16_bf16 a[96:111], v[64:67], v[156:159], a[96:111]
	v_exp_f32_e32 v155, v107
	v_exp_f32_e32 v156, v108
	v_add_f32_e32 v68, v68, v152
	v_add_f32_e32 v69, v69, v153
	v_add_f32_e32 v68, v68, v154
	v_exp_f32_e32 v157, v109
	v_exp_f32_e32 v158, v110
	v_exp_f32_e32 v159, v111
	v_mfma_f32_32x32x16_bf16 a[112:127], v[64:67], v[160:163], a[112:127]
	v_add_f32_e32 v64, v69, v155
	v_add_f32_e32 v65, v68, v156
	s_andn2_b64 vcc, exec, s[0:1]
	v_add_f32_e32 v64, v64, v157
	v_add_f32_e32 v237, v65, v158
	s_nop 0
	v_add_f32_e32 v238, v64, v159
	s_cbranch_vccz .LBB0_25
